# baseline (speedup 1.0000x reference)
_Z11gemm_kernelPKfPKDF16bS0_Pf:
	s_and_b32 s3, s2, 7
	s_ashr_i32 s14, s2, 3
	s_lshl_b32 s12, s3, 6
	s_load_dwordx8 s[4:11], s[0:1], 0x0
	s_add_i32 s12, s12, s14
	s_bfe_u32 s18, s2, 0x10002
	s_lshl_b32 s2, s12, 6
	s_lshl_b32 s13, s18, 14
	s_and_b32 s2, s2, 0x3f00
	v_lshrrev_b32_e32 v52, 6, v0
	v_and_b32_e32 v50, 15, v0
	v_bfe_u32 v51, v0, 4, 2
	v_bfe_u32 v1, v0, 3, 3
	s_or_b32 s2, s2, s13
	v_lshl_or_b32 v102, v52, 2, v51
	v_lshl_or_b32 v104, v52, 3, v1
	v_lshlrev_b32_e32 v1, 4, v50
	s_lshl_b32 s15, s2, 9
	s_waitcnt lgkmcnt(0)
	v_and_b32_e32 v238, 3, v52
	v_lshlrev_b32_e32 v238, 6, v238
	v_lshl_or_b32 v238, v51, 2, v238
	v_lshlrev_b32_e32 v238, 2, v238
	s_and_b32 s24, s12, 3
	s_lshl_b32 s24, s24, 8
	s_lshl_b32 s25, s18, 10
	s_add_u32 s24, s24, s25
	s_lshl_b32 s24, s24, 2
	s_add_u32 s24, s8, s24
	s_addc_u32 s25, s9, 0
	global_load_dwordx4 v[240:243], v238, s[24:25]
	global_load_dwordx4 v[244:247], v238, s[24:25] offset:64
	global_load_dwordx4 v[248:251], v238, s[24:25] offset:128
	global_load_dwordx4 v[252:255], v238, s[24:25] offset:192
	s_mov_b64 s[0:1], s[6:7]
	s_and_b32 s5, s5, 0xffff
	s_mov_b32 s7, 0x20000
	s_brev_b32 s6, -2
	v_lshl_or_b32 v1, v102, 9, v1
	s_or_b32 s2, s15, 0x4000
	s_lshl_b32 s14, s14, 8
	v_lshlrev_b32_e32 v103, 3, v0
	buffer_load_dwordx4 v[54:57], v1, s[4:7], s15 offen sc0 nt
	buffer_load_dwordx4 v[58:61], v1, s[4:7], s2 offen sc0 nt
	s_or_b32 s2, s15, 0x8000
	s_or_b32 s3, s15, 0xc000
	s_lshl_b32 s19, s18, 10
	s_and_b32 s20, s14, 0x300
	v_and_b32_e32 v105, 56, v103
	buffer_load_dwordx4 v[62:65], v1, s[4:7], s2 offen sc0 nt
	buffer_load_dwordx4 v[66:69], v1, s[4:7], s3 offen sc0 nt
	s_or_b32 s2, s15, 0x10000
	s_or_b32 s3, s15, 0x14000
	s_or_b32 s14, s19, s20
	v_lshlrev_b32_e32 v106, 1, v105
	buffer_load_dwordx4 v[70:73], v1, s[4:7], s2 offen sc0 nt
	buffer_load_dwordx4 v[74:77], v1, s[4:7], s3 offen sc0 nt
	s_or_b32 s2, s15, 0x18000
	s_or_b32 s3, s15, 0x1c000
	s_lshl_b32 s14, s14, 11
	buffer_load_dwordx4 v[78:81], v1, s[4:7], s2 offen sc0 nt
	buffer_load_dwordx4 v[82:85], v1, s[4:7], s3 offen sc0 nt
	s_and_b32 s1, s1, 0xffff
	s_mov_b32 s2, s6
	s_mov_b32 s3, s7
	v_lshl_or_b32 v188, v104, 11, v106
	s_or_b32 s16, s14, 0x20000
	buffer_load_dwordx4 v[86:89], v188, s[0:3], s14 offen
	buffer_load_dwordx4 v[90:93], v188, s[0:3], s16 offen
	s_or_b32 s16, s14, 0x40000
	s_or_b32 s17, s14, 0x60000
	buffer_load_dwordx4 v[94:97], v188, s[0:3], s16 offen
	buffer_load_dwordx4 v[98:101], v188, s[0:3], s17 offen
	s_or_b32 s16, s15, 0x100
	s_or_b32 s17, s15, 0x4100
	buffer_load_dwordx4 v[10:13], v1, s[4:7], s16 offen sc0 nt
	buffer_load_dwordx4 v[18:21], v1, s[4:7], s17 offen sc0 nt
	s_or_b32 s16, s15, 0x8100
	s_or_b32 s17, s15, 0xc100
	buffer_load_dwordx4 v[22:25], v1, s[4:7], s16 offen sc0 nt
	buffer_load_dwordx4 v[30:33], v1, s[4:7], s17 offen sc0 nt
	s_or_b32 s16, s15, 0x10100
	s_or_b32 s17, s15, 0x14100
	buffer_load_dwordx4 v[34:37], v1, s[4:7], s16 offen sc0 nt
	buffer_load_dwordx4 v[38:41], v1, s[4:7], s17 offen sc0 nt
	s_or_b32 s16, s15, 0x18100
	s_or_b32 s15, s15, 0x1c100
	buffer_load_dwordx4 v[42:45], v1, s[4:7], s16 offen sc0 nt
	buffer_load_dwordx4 v[46:49], v1, s[4:7], s15 offen sc0 nt
	s_or_b32 s15, s14, 0x80
	s_or_b32 s16, s14, 0x20080
	buffer_load_dwordx4 v[2:5], v188, s[0:3], s15 offen
	buffer_load_dwordx4 v[6:9], v188, s[0:3], s16 offen
	s_or_b32 s15, s14, 0x40080
	s_or_b32 s16, s14, 0x60080
	buffer_load_dwordx4 v[14:17], v188, s[0:3], s15 offen
	buffer_load_dwordx4 v[26:29], v188, s[0:3], s16 offen
	v_lshrrev_b32_e32 v107, 7, v0
	v_bfe_u32 v108, v0, 3, 1
	v_lshlrev_b32_e32 v102, 6, v102
	s_movk_i32 s2, 0x3c0
	v_and_or_b32 v102, v102, s2, v105
	v_lshrrev_b32_e32 v105, 2, v0
	v_and_or_b32 v107, v107, 2, v108
	v_and_b32_e32 v105, 32, v105
	v_lshlrev_b32_e32 v107, 10, v107
	v_bfe_u32 v103, v103, 5, 1
	v_lshlrev_b32_e32 v104, 6, v104
	v_and_b32_e32 v106, 48, v106
	v_bitop3_b32 v189, v102, v107, v105 bitop3:0xde
	v_and_or_b32 v103, v52, 6, v103
	v_and_or_b32 v104, v104, s2, v106
	v_lshrrev_b32_e32 v106, 1, v0
	v_lshlrev_b32_e32 v103, 10, v103
	v_and_b32_e32 v106, 32, v106
	v_bitop3_b32 v190, v104, v103, v106 bitop3:0xde
	v_lshrrev_b32_e32 v53, 8, v0
	s_movk_i32 s15, 0x4000
	s_mov_b32 s16, 0x8000
	s_mov_b32 s17, 0xc000
	s_waitcnt vmcnt(23)
	v_cvt_pk_bf16_f32 v57, v56, v57
	v_cvt_pk_bf16_f32 v56, v54, v55
	s_waitcnt vmcnt(22)
	v_cvt_pk_bf16_f32 v55, v60, v61
	v_cvt_pk_bf16_f32 v54, v58, v59
	ds_write2st64_b64 v189, v[56:57], v[54:55] offset1:8
	s_waitcnt vmcnt(21)
	v_cvt_pk_bf16_f32 v55, v64, v65
	v_cvt_pk_bf16_f32 v54, v62, v63
	s_waitcnt vmcnt(20)
	v_cvt_pk_bf16_f32 v57, v68, v69
	v_cvt_pk_bf16_f32 v56, v66, v67
	ds_write2st64_b64 v189, v[54:55], v[56:57] offset0:16 offset1:24
	s_waitcnt vmcnt(19)
	v_cvt_pk_bf16_f32 v55, v72, v73
	v_cvt_pk_bf16_f32 v54, v70, v71
	s_waitcnt vmcnt(18)
	v_cvt_pk_bf16_f32 v57, v76, v77
	v_cvt_pk_bf16_f32 v56, v74, v75
	ds_write2st64_b64 v189, v[54:55], v[56:57] offset0:32 offset1:40
	s_waitcnt vmcnt(17)
	v_cvt_pk_bf16_f32 v55, v80, v81
	v_cvt_pk_bf16_f32 v54, v78, v79
	s_waitcnt vmcnt(16)
	v_cvt_pk_bf16_f32 v57, v84, v85
	v_cvt_pk_bf16_f32 v56, v82, v83
	ds_write2st64_b64 v189, v[54:55], v[56:57] offset0:48 offset1:56
	s_waitcnt vmcnt(15)
	ds_write_b128 v190, v[86:89] offset:32768
	s_waitcnt vmcnt(14)
	ds_write_b128 v190, v[90:93] offset:40960
	s_waitcnt vmcnt(13)
	ds_write_b128 v190, v[94:97] offset:49152
	s_waitcnt vmcnt(12)
	ds_write_b128 v190, v[98:101] offset:57344
	s_waitcnt lgkmcnt(0)
	s_barrier
	v_cmp_eq_u32_e32 vcc, 1, v53
	s_and_saveexec_b64 s[2:3], vcc
	s_cbranch_execz .LBB1_2
	s_barrier

.LBB1_4:
	v_add_u32_e32 v182, s19, v191
	v_add_u32_e32 v238, s19, v192
	ds_read_b128 v[178:181], v182 offset:32768
	ds_read_b128 v[194:197], v182 offset:34816
	ds_read_b128 v[198:201], v182 offset:36864
	ds_read_b128 v[202:205], v182 offset:38912
	ds_read_b128 v[206:209], v238
	ds_read_b128 v[210:213], v238 offset:2048
	ds_read_b128 v[214:217], v238 offset:4096
	ds_read_b128 v[218:221], v238 offset:6144
	ds_read_b128 v[222:225], v238 offset:8192
	ds_read_b128 v[226:229], v238 offset:10240
	ds_read_b128 v[230:233], v238 offset:12288
	ds_read_b128 v[234:237], v238 offset:14336
	s_min_u32 s21, s20, 29
	s_xor_b32 s19, s19, 0x10000
	v_add_u32_e32 v239, s19, v189
	s_waitcnt vmcnt(11)
	v_cvt_pk_bf16_f32 v13, v12, v13
	v_cvt_pk_bf16_f32 v12, v10, v11
	s_waitcnt vmcnt(10)
	v_cvt_pk_bf16_f32 v11, v20, v21
	v_cvt_pk_bf16_f32 v10, v18, v19
	ds_write2st64_b64 v239, v[12:13], v[10:11] offset1:8
	s_waitcnt vmcnt(9)
	v_cvt_pk_bf16_f32 v11, v24, v25
	v_cvt_pk_bf16_f32 v10, v22, v23
	s_waitcnt vmcnt(8)
	v_cvt_pk_bf16_f32 v13, v32, v33
	v_cvt_pk_bf16_f32 v12, v30, v31
	ds_write2st64_b64 v239, v[10:11], v[12:13] offset0:16 offset1:24
	s_waitcnt vmcnt(7)
	v_cvt_pk_bf16_f32 v11, v36, v37
	v_cvt_pk_bf16_f32 v10, v34, v35
	s_waitcnt vmcnt(6)
	v_cvt_pk_bf16_f32 v13, v40, v41
	v_cvt_pk_bf16_f32 v12, v38, v39
	ds_write2st64_b64 v239, v[10:11], v[12:13] offset0:32 offset1:40
	s_waitcnt vmcnt(5)
	v_cvt_pk_bf16_f32 v11, v44, v45
	v_cvt_pk_bf16_f32 v10, v42, v43
	s_waitcnt vmcnt(4)
	v_cvt_pk_bf16_f32 v13, v48, v49
	v_cvt_pk_bf16_f32 v12, v46, v47
	ds_write2st64_b64 v239, v[10:11], v[12:13] offset0:48 offset1:56
	s_waitcnt lgkmcnt(0)
	s_add_i32 s21, s21, 2
	s_barrier
	s_setprio 1
	s_lshl_b32 s22, s21, 1
	s_and_b32 s22, s22, 0x60
	s_add_i32 s22, s22, s12
	s_lshl_b32 s22, s22, 6
	s_and_b32 s22, s22, 0x3f00
	s_or_b32 s22, s22, s13
	s_lshl_b32 s23, s21, 23
	s_lshl_b32 s22, s22, 9
	s_and_b32 s23, s23, 0x7000000
	s_or_b32 s22, s22, s23
	s_lshl_b32 s23, s21, 8
	s_and_b32 s23, s23, 0x100
	s_or_b32 s22, s22, s23
	s_or_b32 s23, s22, 0x4000
	s_waitcnt lgkmcnt(11)
	v_mfma_f32_16x16x32_bf16 v[174:177], v[178:181], v[206:209], v[174:177]
	v_mfma_f32_16x16x32_bf16 v[170:173], v[194:197], v[206:209], v[170:173]
	v_mfma_f32_16x16x32_bf16 v[158:161], v[198:201], v[206:209], v[158:161]
	buffer_load_dwordx4 v[10:13], v1, s[4:7], s22 offen sc0 nt
	v_mfma_f32_16x16x32_bf16 v[142:145], v[202:205], v[206:209], v[142:145]
	s_waitcnt lgkmcnt(10)
	v_mfma_f32_16x16x32_bf16 v[166:169], v[178:181], v[210:213], v[166:169]
	v_mfma_f32_16x16x32_bf16 v[162:165], v[194:197], v[210:213], v[162:165]
	v_mfma_f32_16x16x32_bf16 v[146:149], v[198:201], v[210:213], v[146:149]
	buffer_load_dwordx4 v[18:21], v1, s[4:7], s23 offen sc0 nt
	s_or_b32 s23, s22, 0x8000
	v_mfma_f32_16x16x32_bf16 v[122:125], v[202:205], v[210:213], v[122:125]
	s_waitcnt lgkmcnt(9)
	v_mfma_f32_16x16x32_bf16 v[154:157], v[178:181], v[214:217], v[154:157]
	v_mfma_f32_16x16x32_bf16 v[150:153], v[194:197], v[214:217], v[150:153]
	v_mfma_f32_16x16x32_bf16 v[130:133], v[198:201], v[214:217], v[130:133]
	buffer_load_dwordx4 v[22:25], v1, s[4:7], s23 offen sc0 nt
	s_or_b32 s23, s22, 0xc000
	v_mfma_f32_16x16x32_bf16 v[106:109], v[202:205], v[214:217], v[106:109]
	s_waitcnt lgkmcnt(8)
	v_mfma_f32_16x16x32_bf16 v[138:141], v[178:181], v[218:221], v[138:141]
	v_mfma_f32_16x16x32_bf16 v[134:137], v[194:197], v[218:221], v[134:137]
	v_mfma_f32_16x16x32_bf16 v[114:117], v[198:201], v[218:221], v[114:117]
	buffer_load_dwordx4 v[30:33], v1, s[4:7], s23 offen sc0 nt
	s_or_b32 s23, s22, 0x10000
	v_mfma_f32_16x16x32_bf16 v[90:93], v[202:205], v[218:221], v[90:93]
	s_waitcnt lgkmcnt(7)
	v_mfma_f32_16x16x32_bf16 v[126:129], v[178:181], v[222:225], v[126:129]
	v_mfma_f32_16x16x32_bf16 v[118:121], v[194:197], v[222:225], v[118:121]
	v_mfma_f32_16x16x32_bf16 v[98:101], v[198:201], v[222:225], v[98:101]
	buffer_load_dwordx4 v[34:37], v1, s[4:7], s23 offen sc0 nt
	s_or_b32 s23, s22, 0x14000
	v_mfma_f32_16x16x32_bf16 v[74:77], v[202:205], v[222:225], v[74:77]
	s_waitcnt lgkmcnt(6)
	v_mfma_f32_16x16x32_bf16 v[110:113], v[178:181], v[226:229], v[110:113]
	v_mfma_f32_16x16x32_bf16 v[102:105], v[194:197], v[226:229], v[102:105]
	v_mfma_f32_16x16x32_bf16 v[82:85], v[198:201], v[226:229], v[82:85]
	buffer_load_dwordx4 v[38:41], v1, s[4:7], s23 offen sc0 nt
	s_or_b32 s23, s22, 0x18000
	s_or_b32 s22, s22, 0x1c000
	v_mfma_f32_16x16x32_bf16 v[62:65], v[202:205], v[226:229], v[62:65]
	s_waitcnt lgkmcnt(5)
	v_mfma_f32_16x16x32_bf16 v[94:97], v[178:181], v[230:233], v[94:97]
	v_mfma_f32_16x16x32_bf16 v[86:89], v[194:197], v[230:233], v[86:89]
	v_mfma_f32_16x16x32_bf16 v[70:73], v[198:201], v[230:233], v[70:73]
	buffer_load_dwordx4 v[42:45], v1, s[4:7], s23 offen sc0 nt
	v_mfma_f32_16x16x32_bf16 v[54:57], v[202:205], v[230:233], v[54:57]
	s_waitcnt lgkmcnt(4)
	v_mfma_f32_16x16x32_bf16 v[78:81], v[178:181], v[234:237], v[78:81]
	v_mfma_f32_16x16x32_bf16 v[66:69], v[194:197], v[234:237], v[66:69]
	v_mfma_f32_16x16x32_bf16 v[58:61], v[198:201], v[234:237], v[58:61]
	buffer_load_dwordx4 v[46:49], v1, s[4:7], s22 offen sc0 nt
	v_mfma_f32_16x16x32_bf16 v[50:53], v[202:205], v[234:237], v[50:53]
	s_setprio 0
	s_waitcnt lgkmcnt(0)
	s_barrier
	ds_read_b128 v[178:181], v182 offset:33792
	ds_read_b128 v[194:197], v182 offset:35840
	ds_read_b128 v[198:201], v182 offset:37888
	ds_read_b128 v[202:205], v182 offset:39936
	ds_read_b128 v[206:209], v238 offset:1024
	ds_read_b128 v[210:213], v238 offset:3072
	ds_read_b128 v[214:217], v238 offset:5120
	ds_read_b128 v[218:221], v238 offset:7168
	ds_read_b128 v[222:225], v238 offset:9216
	ds_read_b128 v[226:229], v238 offset:11264
	ds_read_b128 v[230:233], v238 offset:13312
	ds_read_b128 v[234:237], v238 offset:15360
	v_add_u32_e32 v182, s19, v190
	s_waitcnt vmcnt(11)
	ds_write_b128 v182, v[2:5] offset:32768
	s_waitcnt vmcnt(10)
	ds_write_b128 v182, v[6:9] offset:40960
	s_waitcnt vmcnt(9)
	ds_write_b128 v182, v[14:17] offset:49152
	s_waitcnt vmcnt(8)
	ds_write_b128 v182, v[26:29] offset:57344
	s_waitcnt lgkmcnt(0)
	s_barrier
	s_setprio 1
	s_lshl_b32 s21, s21, 7
	s_and_b32 s21, s21, 0x780
	s_or_b32 s21, s21, s14
	s_or_b32 s22, s21, 0x20000
	s_waitcnt lgkmcnt(11)
	v_mfma_f32_16x16x32_bf16 v[174:177], v[178:181], v[206:209], v[174:177]
	v_mfma_f32_16x16x32_bf16 v[170:173], v[194:197], v[206:209], v[170:173]
	v_mfma_f32_16x16x32_bf16 v[158:161], v[198:201], v[206:209], v[158:161]
	v_mfma_f32_16x16x32_bf16 v[142:145], v[202:205], v[206:209], v[142:145]
	s_waitcnt lgkmcnt(10)
	v_mfma_f32_16x16x32_bf16 v[166:169], v[178:181], v[210:213], v[166:169]
	v_mfma_f32_16x16x32_bf16 v[162:165], v[194:197], v[210:213], v[162:165]
	buffer_load_dwordx4 v[2:5], v188, s[0:3], s21 offen
	v_mfma_f32_16x16x32_bf16 v[146:149], v[198:201], v[210:213], v[146:149]
	v_mfma_f32_16x16x32_bf16 v[122:125], v[202:205], v[210:213], v[122:125]
	s_waitcnt lgkmcnt(9)
	v_mfma_f32_16x16x32_bf16 v[154:157], v[178:181], v[214:217], v[154:157]
	v_mfma_f32_16x16x32_bf16 v[150:153], v[194:197], v[214:217], v[150:153]
	v_mfma_f32_16x16x32_bf16 v[130:133], v[198:201], v[214:217], v[130:133]
	v_mfma_f32_16x16x32_bf16 v[106:109], v[202:205], v[214:217], v[106:109]
	s_waitcnt lgkmcnt(8)
	v_mfma_f32_16x16x32_bf16 v[138:141], v[178:181], v[218:221], v[138:141]
	v_mfma_f32_16x16x32_bf16 v[134:137], v[194:197], v[218:221], v[134:137]
	buffer_load_dwordx4 v[6:9], v188, s[0:3], s22 offen
	s_or_b32 s22, s21, 0x40000
	s_or_b32 s21, s21, 0x60000
	v_mfma_f32_16x16x32_bf16 v[114:117], v[198:201], v[218:221], v[114:117]
	v_mfma_f32_16x16x32_bf16 v[90:93], v[202:205], v[218:221], v[90:93]
	s_waitcnt lgkmcnt(7)
	v_mfma_f32_16x16x32_bf16 v[126:129], v[178:181], v[222:225], v[126:129]
	v_mfma_f32_16x16x32_bf16 v[118:121], v[194:197], v[222:225], v[118:121]
	v_mfma_f32_16x16x32_bf16 v[98:101], v[198:201], v[222:225], v[98:101]
	v_mfma_f32_16x16x32_bf16 v[74:77], v[202:205], v[222:225], v[74:77]
	s_waitcnt lgkmcnt(6)
	v_mfma_f32_16x16x32_bf16 v[110:113], v[178:181], v[226:229], v[110:113]
	v_mfma_f32_16x16x32_bf16 v[102:105], v[194:197], v[226:229], v[102:105]
	buffer_load_dwordx4 v[14:17], v188, s[0:3], s22 offen
	v_mfma_f32_16x16x32_bf16 v[82:85], v[198:201], v[226:229], v[82:85]
	v_mfma_f32_16x16x32_bf16 v[62:65], v[202:205], v[226:229], v[62:65]
	s_waitcnt lgkmcnt(5)
	v_mfma_f32_16x16x32_bf16 v[94:97], v[178:181], v[230:233], v[94:97]
	v_mfma_f32_16x16x32_bf16 v[86:89], v[194:197], v[230:233], v[86:89]
	v_mfma_f32_16x16x32_bf16 v[70:73], v[198:201], v[230:233], v[70:73]
	v_mfma_f32_16x16x32_bf16 v[54:57], v[202:205], v[230:233], v[54:57]
	s_waitcnt lgkmcnt(4)
	v_mfma_f32_16x16x32_bf16 v[78:81], v[178:181], v[234:237], v[78:81]
	v_mfma_f32_16x16x32_bf16 v[66:69], v[194:197], v[234:237], v[66:69]
	buffer_load_dwordx4 v[26:29], v188, s[0:3], s21 offen
	v_mfma_f32_16x16x32_bf16 v[58:61], v[198:201], v[234:237], v[58:61]
	v_mfma_f32_16x16x32_bf16 v[50:53], v[202:205], v[234:237], v[50:53]
	s_setprio 0
	s_and_b32 s21, s20, 15
	s_cmp_lg_u32 s21, 15
	s_cbranch_scc1 .LBB1_3
	s_and_b32 s21, s18, 32
	s_add_i32 s21, s21, s12
	s_lshl_b32 s21, s21, 6
	s_and_b32 s21, s21, 0x3f00
	v_add_lshl_u32 v182, v193, s21, 9
	v_lshl_add_u64 v[206:207], v[184:185], 0, v[182:183]
	v_add_co_u32_e32 v208, vcc, s8, v206
	s_nop 1
	v_addc_co_u32_e32 v209, vcc, 0, v207, vcc
	v_add_co_u32_e32 v210, vcc, s15, v206
	s_nop 1
	v_addc_co_u32_e32 v211, vcc, 0, v207, vcc
	v_add_co_u32_e32 v212, vcc, s9, v206
	s_nop 1
	v_addc_co_u32_e32 v213, vcc, 0, v207, vcc
	v_add_co_u32_e32 v214, vcc, s16, v206
	s_nop 1
	v_addc_co_u32_e32 v215, vcc, 0, v207, vcc
	v_add_co_u32_e32 v216, vcc, s10, v206
	s_nop 1
	v_addc_co_u32_e32 v217, vcc, 0, v207, vcc
	v_add_co_u32_e32 v218, vcc, s17, v206
	s_nop 1
	v_addc_co_u32_e32 v219, vcc, 0, v207, vcc
	v_add_co_u32_e32 v220, vcc, s11, v206
	s_nop 1
	v_addc_co_u32_e32 v221, vcc, 0, v207, vcc
	global_store_dwordx4 v[206:207], v[174:177], off
	global_store_dwordx4 v[206:207], v[170:173], off offset:64
	global_store_dwordx4 v[206:207], v[158:161], off offset:128
	global_store_dwordx4 v[206:207], v[142:145], off offset:192
	global_store_dwordx4 v[208:209], v[166:169], off
	global_store_dwordx4 v[208:209], v[162:165], off offset:64
	global_store_dwordx4 v[208:209], v[146:149], off offset:128
	global_store_dwordx4 v[208:209], v[122:125], off offset:192
	global_store_dwordx4 v[210:211], v[154:157], off
	global_store_dwordx4 v[210:211], v[150:153], off offset:64
	global_store_dwordx4 v[210:211], v[130:133], off offset:128
	global_store_dwordx4 v[210:211], v[106:109], off offset:192
	global_store_dwordx4 v[212:213], v[138:141], off
	global_store_dwordx4 v[212:213], v[134:137], off offset:64
	global_store_dwordx4 v[212:213], v[114:117], off offset:128
	global_store_dwordx4 v[212:213], v[90:93], off offset:192
	global_store_dwordx4 v[214:215], v[126:129], off
	global_store_dwordx4 v[214:215], v[118:121], off offset:64
	global_store_dwordx4 v[214:215], v[98:101], off offset:128
	global_store_dwordx4 v[214:215], v[74:77], off offset:192
	global_store_dwordx4 v[216:217], v[110:113], off
	global_store_dwordx4 v[216:217], v[102:105], off offset:64
	global_store_dwordx4 v[216:217], v[82:85], off offset:128
	global_store_dwordx4 v[216:217], v[62:65], off offset:192
	global_store_dwordx4 v[218:219], v[94:97], off
	global_store_dwordx4 v[218:219], v[86:89], off offset:64
	global_store_dwordx4 v[218:219], v[70:73], off offset:128
	global_store_dwordx4 v[218:219], v[54:57], off offset:192
	global_store_dwordx4 v[220:221], v[78:81], off
	global_store_dwordx4 v[220:221], v[66:69], off offset:64
	global_store_dwordx4 v[220:221], v[58:61], off offset:128
	global_store_dwordx4 v[220:221], v[50:53], off offset:192
.Lpd_tail:
	s_waitcnt lgkmcnt(0)
	s_barrier
	s_add_i32 s20, s20, 1
	s_add_i32 s18, s18, 2
	v_add_u32_e32 v182, s19, v191
	v_add_u32_e32 v238, s19, v192
	ds_read_b128 v[178:181], v182 offset:32768
	ds_read_b128 v[194:197], v182 offset:34816
	ds_read_b128 v[198:201], v182 offset:36864
	ds_read_b128 v[202:205], v182 offset:38912
	ds_read_b128 v[206:209], v238
	ds_read_b128 v[210:213], v238 offset:2048
	ds_read_b128 v[214:217], v238 offset:4096
	ds_read_b128 v[218:221], v238 offset:6144
	ds_read_b128 v[222:225], v238 offset:8192
	ds_read_b128 v[226:229], v238 offset:10240
	ds_read_b128 v[230:233], v238 offset:12288
	ds_read_b128 v[234:237], v238 offset:14336
	s_min_u32 s21, s20, 29
	s_xor_b32 s19, s19, 0x10000
	v_add_u32_e32 v239, s19, v189
	s_waitcnt vmcnt(43)
	v_cvt_pk_bf16_f32 v13, v12, v13
	v_cvt_pk_bf16_f32 v12, v10, v11
	s_waitcnt vmcnt(42)
	v_cvt_pk_bf16_f32 v11, v20, v21
	v_cvt_pk_bf16_f32 v10, v18, v19
	ds_write2st64_b64 v239, v[12:13], v[10:11] offset1:8
	s_waitcnt vmcnt(41)
	v_cvt_pk_bf16_f32 v11, v24, v25
	v_cvt_pk_bf16_f32 v10, v22, v23
	s_waitcnt vmcnt(40)
	v_cvt_pk_bf16_f32 v13, v32, v33
	v_cvt_pk_bf16_f32 v12, v30, v31
	ds_write2st64_b64 v239, v[10:11], v[12:13] offset0:16 offset1:24
	s_waitcnt vmcnt(39)
	v_cvt_pk_bf16_f32 v11, v36, v37
	v_cvt_pk_bf16_f32 v10, v34, v35
	s_waitcnt vmcnt(38)
	v_cvt_pk_bf16_f32 v13, v40, v41
	v_cvt_pk_bf16_f32 v12, v38, v39
	ds_write2st64_b64 v239, v[10:11], v[12:13] offset0:32 offset1:40
	s_waitcnt vmcnt(37)
	v_cvt_pk_bf16_f32 v11, v44, v45
	v_cvt_pk_bf16_f32 v10, v42, v43
	s_waitcnt vmcnt(36)
	v_cvt_pk_bf16_f32 v13, v48, v49
	v_cvt_pk_bf16_f32 v12, v46, v47
	ds_write2st64_b64 v239, v[10:11], v[12:13] offset0:48 offset1:56
	s_waitcnt lgkmcnt(0)
	s_add_i32 s21, s21, 2
	s_barrier
	s_setprio 1
	s_lshl_b32 s22, s21, 1
	s_and_b32 s22, s22, 0x60
	s_add_i32 s22, s22, s12
	s_lshl_b32 s22, s22, 6
	s_and_b32 s22, s22, 0x3f00
	s_or_b32 s22, s22, s13
	s_lshl_b32 s23, s21, 23
	s_lshl_b32 s22, s22, 9
	s_and_b32 s23, s23, 0x7000000
	s_or_b32 s22, s22, s23
	s_lshl_b32 s23, s21, 8
	s_and_b32 s23, s23, 0x100
	s_or_b32 s22, s22, s23
	s_or_b32 s23, s22, 0x4000
	s_waitcnt lgkmcnt(11)
	v_mfma_f32_16x16x32_bf16 v[174:177], v[178:181], v[206:209], v[240:243]
	v_mfma_f32_16x16x32_bf16 v[170:173], v[194:197], v[206:209], v[244:247]
	v_mfma_f32_16x16x32_bf16 v[158:161], v[198:201], v[206:209], v[248:251]
	buffer_load_dwordx4 v[10:13], v1, s[4:7], s22 offen sc0 nt
	v_mfma_f32_16x16x32_bf16 v[142:145], v[202:205], v[206:209], v[252:255]
	s_waitcnt lgkmcnt(10)
	v_mfma_f32_16x16x32_bf16 v[166:169], v[178:181], v[210:213], v[240:243]
	v_mfma_f32_16x16x32_bf16 v[162:165], v[194:197], v[210:213], v[244:247]
	v_mfma_f32_16x16x32_bf16 v[146:149], v[198:201], v[210:213], v[248:251]
	buffer_load_dwordx4 v[18:21], v1, s[4:7], s23 offen sc0 nt
	s_or_b32 s23, s22, 0x8000
	v_mfma_f32_16x16x32_bf16 v[122:125], v[202:205], v[210:213], v[252:255]
	s_waitcnt lgkmcnt(9)
	v_mfma_f32_16x16x32_bf16 v[154:157], v[178:181], v[214:217], v[240:243]
	v_mfma_f32_16x16x32_bf16 v[150:153], v[194:197], v[214:217], v[244:247]
	v_mfma_f32_16x16x32_bf16 v[130:133], v[198:201], v[214:217], v[248:251]
	buffer_load_dwordx4 v[22:25], v1, s[4:7], s23 offen sc0 nt
	s_or_b32 s23, s22, 0xc000
	v_mfma_f32_16x16x32_bf16 v[106:109], v[202:205], v[214:217], v[252:255]
	s_waitcnt lgkmcnt(8)
	v_mfma_f32_16x16x32_bf16 v[138:141], v[178:181], v[218:221], v[240:243]
	v_mfma_f32_16x16x32_bf16 v[134:137], v[194:197], v[218:221], v[244:247]
	v_mfma_f32_16x16x32_bf16 v[114:117], v[198:201], v[218:221], v[248:251]
	buffer_load_dwordx4 v[30:33], v1, s[4:7], s23 offen sc0 nt
	s_or_b32 s23, s22, 0x10000
	v_mfma_f32_16x16x32_bf16 v[90:93], v[202:205], v[218:221], v[252:255]
	s_waitcnt lgkmcnt(7)
	v_mfma_f32_16x16x32_bf16 v[126:129], v[178:181], v[222:225], v[240:243]
	v_mfma_f32_16x16x32_bf16 v[118:121], v[194:197], v[222:225], v[244:247]
	v_mfma_f32_16x16x32_bf16 v[98:101], v[198:201], v[222:225], v[248:251]
	buffer_load_dwordx4 v[34:37], v1, s[4:7], s23 offen sc0 nt
	s_or_b32 s23, s22, 0x14000
	v_mfma_f32_16x16x32_bf16 v[74:77], v[202:205], v[222:225], v[252:255]
	s_waitcnt lgkmcnt(6)
	v_mfma_f32_16x16x32_bf16 v[110:113], v[178:181], v[226:229], v[240:243]
	v_mfma_f32_16x16x32_bf16 v[102:105], v[194:197], v[226:229], v[244:247]
	v_mfma_f32_16x16x32_bf16 v[82:85], v[198:201], v[226:229], v[248:251]
	buffer_load_dwordx4 v[38:41], v1, s[4:7], s23 offen sc0 nt
	s_or_b32 s23, s22, 0x18000
	s_or_b32 s22, s22, 0x1c000
	v_mfma_f32_16x16x32_bf16 v[62:65], v[202:205], v[226:229], v[252:255]
	s_waitcnt lgkmcnt(5)
	v_mfma_f32_16x16x32_bf16 v[94:97], v[178:181], v[230:233], v[240:243]
	v_mfma_f32_16x16x32_bf16 v[86:89], v[194:197], v[230:233], v[244:247]
	v_mfma_f32_16x16x32_bf16 v[70:73], v[198:201], v[230:233], v[248:251]
	buffer_load_dwordx4 v[42:45], v1, s[4:7], s23 offen sc0 nt
	v_mfma_f32_16x16x32_bf16 v[54:57], v[202:205], v[230:233], v[252:255]
	s_waitcnt lgkmcnt(4)
	v_mfma_f32_16x16x32_bf16 v[78:81], v[178:181], v[234:237], v[240:243]
	v_mfma_f32_16x16x32_bf16 v[66:69], v[194:197], v[234:237], v[244:247]
	v_mfma_f32_16x16x32_bf16 v[58:61], v[198:201], v[234:237], v[248:251]
	buffer_load_dwordx4 v[46:49], v1, s[4:7], s22 offen sc0 nt
	v_mfma_f32_16x16x32_bf16 v[50:53], v[202:205], v[234:237], v[252:255]
	s_setprio 0
	s_waitcnt lgkmcnt(0)
	s_barrier
	ds_read_b128 v[178:181], v182 offset:33792
	ds_read_b128 v[194:197], v182 offset:35840
	ds_read_b128 v[198:201], v182 offset:37888
	ds_read_b128 v[202:205], v182 offset:39936
	ds_read_b128 v[206:209], v238 offset:1024
	ds_read_b128 v[210:213], v238 offset:3072
	ds_read_b128 v[214:217], v238 offset:5120
	ds_read_b128 v[218:221], v238 offset:7168
	ds_read_b128 v[222:225], v238 offset:9216
	ds_read_b128 v[226:229], v238 offset:11264
	ds_read_b128 v[230:233], v238 offset:13312
	ds_read_b128 v[234:237], v238 offset:15360
	v_add_u32_e32 v182, s19, v190
	s_waitcnt vmcnt(43)
	ds_write_b128 v182, v[2:5] offset:32768
	s_waitcnt vmcnt(42)
	ds_write_b128 v182, v[6:9] offset:40960
	s_waitcnt vmcnt(41)
	ds_write_b128 v182, v[14:17] offset:49152
	s_waitcnt vmcnt(40)
	ds_write_b128 v182, v[26:29] offset:57344
	s_waitcnt lgkmcnt(0)
	s_barrier
	s_setprio 1
	s_lshl_b32 s21, s21, 7
	s_and_b32 s21, s21, 0x780
	s_or_b32 s21, s21, s14
	s_or_b32 s22, s21, 0x20000
	s_waitcnt lgkmcnt(11)
	v_mfma_f32_16x16x32_bf16 v[174:177], v[178:181], v[206:209], v[174:177]
	v_mfma_f32_16x16x32_bf16 v[170:173], v[194:197], v[206:209], v[170:173]
	v_mfma_f32_16x16x32_bf16 v[158:161], v[198:201], v[206:209], v[158:161]
	v_mfma_f32_16x16x32_bf16 v[142:145], v[202:205], v[206:209], v[142:145]
	s_waitcnt lgkmcnt(10)
	v_mfma_f32_16x16x32_bf16 v[166:169], v[178:181], v[210:213], v[166:169]
	v_mfma_f32_16x16x32_bf16 v[162:165], v[194:197], v[210:213], v[162:165]
	buffer_load_dwordx4 v[2:5], v188, s[0:3], s21 offen
	v_mfma_f32_16x16x32_bf16 v[146:149], v[198:201], v[210:213], v[146:149]
	v_mfma_f32_16x16x32_bf16 v[122:125], v[202:205], v[210:213], v[122:125]
	s_waitcnt lgkmcnt(9)
	v_mfma_f32_16x16x32_bf16 v[154:157], v[178:181], v[214:217], v[154:157]
	v_mfma_f32_16x16x32_bf16 v[150:153], v[194:197], v[214:217], v[150:153]
	v_mfma_f32_16x16x32_bf16 v[130:133], v[198:201], v[214:217], v[130:133]
	v_mfma_f32_16x16x32_bf16 v[106:109], v[202:205], v[214:217], v[106:109]
	s_waitcnt lgkmcnt(8)
	v_mfma_f32_16x16x32_bf16 v[138:141], v[178:181], v[218:221], v[138:141]
	v_mfma_f32_16x16x32_bf16 v[134:137], v[194:197], v[218:221], v[134:137]
	buffer_load_dwordx4 v[6:9], v188, s[0:3], s22 offen
	s_or_b32 s22, s21, 0x40000
	s_or_b32 s21, s21, 0x60000
	v_mfma_f32_16x16x32_bf16 v[114:117], v[198:201], v[218:221], v[114:117]
	v_mfma_f32_16x16x32_bf16 v[90:93], v[202:205], v[218:221], v[90:93]
	s_waitcnt lgkmcnt(7)
	v_mfma_f32_16x16x32_bf16 v[126:129], v[178:181], v[222:225], v[126:129]
	v_mfma_f32_16x16x32_bf16 v[118:121], v[194:197], v[222:225], v[118:121]
	v_mfma_f32_16x16x32_bf16 v[98:101], v[198:201], v[222:225], v[98:101]
	v_mfma_f32_16x16x32_bf16 v[74:77], v[202:205], v[222:225], v[74:77]
	s_waitcnt lgkmcnt(6)
	v_mfma_f32_16x16x32_bf16 v[110:113], v[178:181], v[226:229], v[110:113]
	v_mfma_f32_16x16x32_bf16 v[102:105], v[194:197], v[226:229], v[102:105]
	buffer_load_dwordx4 v[14:17], v188, s[0:3], s22 offen
	v_mfma_f32_16x16x32_bf16 v[82:85], v[198:201], v[226:229], v[82:85]
	v_mfma_f32_16x16x32_bf16 v[62:65], v[202:205], v[226:229], v[62:65]
	s_waitcnt lgkmcnt(5)
	v_mfma_f32_16x16x32_bf16 v[94:97], v[178:181], v[230:233], v[94:97]
	v_mfma_f32_16x16x32_bf16 v[86:89], v[194:197], v[230:233], v[86:89]
	v_mfma_f32_16x16x32_bf16 v[70:73], v[198:201], v[230:233], v[70:73]
	v_mfma_f32_16x16x32_bf16 v[54:57], v[202:205], v[230:233], v[54:57]
	s_waitcnt lgkmcnt(4)
	v_mfma_f32_16x16x32_bf16 v[78:81], v[178:181], v[234:237], v[78:81]
	v_mfma_f32_16x16x32_bf16 v[66:69], v[194:197], v[234:237], v[66:69]
	buffer_load_dwordx4 v[26:29], v188, s[0:3], s21 offen
	v_mfma_f32_16x16x32_bf16 v[58:61], v[198:201], v[234:237], v[58:61]
	v_mfma_f32_16x16x32_bf16 v[50:53], v[202:205], v[234:237], v[50:53]
	s_setprio 0
	s_branch .LBB1_3

.Lfirst:
	v_add_u32_e32 v182, s19, v191
	v_add_u32_e32 v238, s19, v192
	ds_read_b128 v[178:181], v182 offset:32768
	ds_read_b128 v[194:197], v182 offset:34816
	ds_read_b128 v[198:201], v182 offset:36864
	ds_read_b128 v[202:205], v182 offset:38912
	ds_read_b128 v[206:209], v238
	ds_read_b128 v[210:213], v238 offset:2048
	ds_read_b128 v[214:217], v238 offset:4096
	ds_read_b128 v[218:221], v238 offset:6144
	ds_read_b128 v[222:225], v238 offset:8192
	ds_read_b128 v[226:229], v238 offset:10240
	ds_read_b128 v[230:233], v238 offset:12288
	ds_read_b128 v[234:237], v238 offset:14336
	s_min_u32 s21, s20, 29
	s_xor_b32 s19, s19, 0x10000
	v_add_u32_e32 v239, s19, v189
	s_waitcnt vmcnt(11)
	v_cvt_pk_bf16_f32 v13, v12, v13
	v_cvt_pk_bf16_f32 v12, v10, v11
	s_waitcnt vmcnt(10)
	v_cvt_pk_bf16_f32 v11, v20, v21
	v_cvt_pk_bf16_f32 v10, v18, v19
	ds_write2st64_b64 v239, v[12:13], v[10:11] offset1:8
	s_waitcnt vmcnt(9)
	v_cvt_pk_bf16_f32 v11, v24, v25
	v_cvt_pk_bf16_f32 v10, v22, v23
	s_waitcnt vmcnt(8)
	v_cvt_pk_bf16_f32 v13, v32, v33
	v_cvt_pk_bf16_f32 v12, v30, v31
	ds_write2st64_b64 v239, v[10:11], v[12:13] offset0:16 offset1:24
	s_waitcnt vmcnt(7)
	v_cvt_pk_bf16_f32 v11, v36, v37
	v_cvt_pk_bf16_f32 v10, v34, v35
	s_waitcnt vmcnt(6)
	v_cvt_pk_bf16_f32 v13, v40, v41
	v_cvt_pk_bf16_f32 v12, v38, v39
	ds_write2st64_b64 v239, v[10:11], v[12:13] offset0:32 offset1:40
	s_waitcnt vmcnt(5)
	v_cvt_pk_bf16_f32 v11, v44, v45
	v_cvt_pk_bf16_f32 v10, v42, v43
	s_waitcnt vmcnt(4)
	v_cvt_pk_bf16_f32 v13, v48, v49
	v_cvt_pk_bf16_f32 v12, v46, v47
	ds_write2st64_b64 v239, v[10:11], v[12:13] offset0:48 offset1:56
	s_waitcnt lgkmcnt(0)
	s_add_i32 s21, s21, 2
	s_barrier
	s_setprio 1
	s_lshl_b32 s22, s21, 1
	s_and_b32 s22, s22, 0x60
	s_add_i32 s22, s22, s12
	s_lshl_b32 s22, s22, 6
	s_and_b32 s22, s22, 0x3f00
	s_or_b32 s22, s22, s13
	s_lshl_b32 s23, s21, 23
	s_lshl_b32 s22, s22, 9
	s_and_b32 s23, s23, 0x7000000
	s_or_b32 s22, s22, s23
	s_lshl_b32 s23, s21, 8
	s_and_b32 s23, s23, 0x100
	s_or_b32 s22, s22, s23
	s_or_b32 s23, s22, 0x4000
	s_waitcnt lgkmcnt(11)
	v_mfma_f32_16x16x32_bf16 v[174:177], v[178:181], v[206:209], v[240:243]
	v_mfma_f32_16x16x32_bf16 v[170:173], v[194:197], v[206:209], v[244:247]
	v_mfma_f32_16x16x32_bf16 v[158:161], v[198:201], v[206:209], v[248:251]
	buffer_load_dwordx4 v[10:13], v1, s[4:7], s22 offen sc0 nt
	v_mfma_f32_16x16x32_bf16 v[142:145], v[202:205], v[206:209], v[252:255]
	s_waitcnt lgkmcnt(10)
	v_mfma_f32_16x16x32_bf16 v[166:169], v[178:181], v[210:213], v[240:243]
	v_mfma_f32_16x16x32_bf16 v[162:165], v[194:197], v[210:213], v[244:247]
	v_mfma_f32_16x16x32_bf16 v[146:149], v[198:201], v[210:213], v[248:251]
	buffer_load_dwordx4 v[18:21], v1, s[4:7], s23 offen sc0 nt
	s_or_b32 s23, s22, 0x8000
	v_mfma_f32_16x16x32_bf16 v[122:125], v[202:205], v[210:213], v[252:255]
	s_waitcnt lgkmcnt(9)
	v_mfma_f32_16x16x32_bf16 v[154:157], v[178:181], v[214:217], v[240:243]
	v_mfma_f32_16x16x32_bf16 v[150:153], v[194:197], v[214:217], v[244:247]
	v_mfma_f32_16x16x32_bf16 v[130:133], v[198:201], v[214:217], v[248:251]
	buffer_load_dwordx4 v[22:25], v1, s[4:7], s23 offen sc0 nt
	s_or_b32 s23, s22, 0xc000
	v_mfma_f32_16x16x32_bf16 v[106:109], v[202:205], v[214:217], v[252:255]
	s_waitcnt lgkmcnt(8)
	v_mfma_f32_16x16x32_bf16 v[138:141], v[178:181], v[218:221], v[240:243]
	v_mfma_f32_16x16x32_bf16 v[134:137], v[194:197], v[218:221], v[244:247]
	v_mfma_f32_16x16x32_bf16 v[114:117], v[198:201], v[218:221], v[248:251]
	buffer_load_dwordx4 v[30:33], v1, s[4:7], s23 offen sc0 nt
	s_or_b32 s23, s22, 0x10000
	v_mfma_f32_16x16x32_bf16 v[90:93], v[202:205], v[218:221], v[252:255]
	s_waitcnt lgkmcnt(7)
	v_mfma_f32_16x16x32_bf16 v[126:129], v[178:181], v[222:225], v[240:243]
	v_mfma_f32_16x16x32_bf16 v[118:121], v[194:197], v[222:225], v[244:247]
	v_mfma_f32_16x16x32_bf16 v[98:101], v[198:201], v[222:225], v[248:251]
	buffer_load_dwordx4 v[34:37], v1, s[4:7], s23 offen sc0 nt
	s_or_b32 s23, s22, 0x14000
	v_mfma_f32_16x16x32_bf16 v[74:77], v[202:205], v[222:225], v[252:255]
	s_waitcnt lgkmcnt(6)
	v_mfma_f32_16x16x32_bf16 v[110:113], v[178:181], v[226:229], v[240:243]
	v_mfma_f32_16x16x32_bf16 v[102:105], v[194:197], v[226:229], v[244:247]
	v_mfma_f32_16x16x32_bf16 v[82:85], v[198:201], v[226:229], v[248:251]
	buffer_load_dwordx4 v[38:41], v1, s[4:7], s23 offen sc0 nt
	s_or_b32 s23, s22, 0x18000
	s_or_b32 s22, s22, 0x1c000
	v_mfma_f32_16x16x32_bf16 v[62:65], v[202:205], v[226:229], v[252:255]
	s_waitcnt lgkmcnt(5)
	v_mfma_f32_16x16x32_bf16 v[94:97], v[178:181], v[230:233], v[240:243]
	v_mfma_f32_16x16x32_bf16 v[86:89], v[194:197], v[230:233], v[244:247]
	v_mfma_f32_16x16x32_bf16 v[70:73], v[198:201], v[230:233], v[248:251]
	buffer_load_dwordx4 v[42:45], v1, s[4:7], s23 offen sc0 nt
	v_mfma_f32_16x16x32_bf16 v[54:57], v[202:205], v[230:233], v[252:255]
	s_waitcnt lgkmcnt(4)
	v_mfma_f32_16x16x32_bf16 v[78:81], v[178:181], v[234:237], v[240:243]
	v_mfma_f32_16x16x32_bf16 v[66:69], v[194:197], v[234:237], v[244:247]
	v_mfma_f32_16x16x32_bf16 v[58:61], v[198:201], v[234:237], v[248:251]
	buffer_load_dwordx4 v[46:49], v1, s[4:7], s22 offen sc0 nt
	v_mfma_f32_16x16x32_bf16 v[50:53], v[202:205], v[234:237], v[252:255]
	s_setprio 0
	s_waitcnt lgkmcnt(0)
	s_barrier
	ds_read_b128 v[178:181], v182 offset:33792
	ds_read_b128 v[194:197], v182 offset:35840
	ds_read_b128 v[198:201], v182 offset:37888
	ds_read_b128 v[202:205], v182 offset:39936
	ds_read_b128 v[206:209], v238 offset:1024
	ds_read_b128 v[210:213], v238 offset:3072
	ds_read_b128 v[214:217], v238 offset:5120
	ds_read_b128 v[218:221], v238 offset:7168
	ds_read_b128 v[222:225], v238 offset:9216
	ds_read_b128 v[226:229], v238 offset:11264
	ds_read_b128 v[230:233], v238 offset:13312
	ds_read_b128 v[234:237], v238 offset:15360
	v_add_u32_e32 v182, s19, v190
	s_waitcnt vmcnt(11)
	ds_write_b128 v182, v[2:5] offset:32768
	s_waitcnt vmcnt(10)
	ds_write_b128 v182, v[6:9] offset:40960
	s_waitcnt vmcnt(9)
	ds_write_b128 v182, v[14:17] offset:49152
	s_waitcnt vmcnt(8)
	ds_write_b128 v182, v[26:29] offset:57344
	s_waitcnt lgkmcnt(0)
	s_barrier
	s_setprio 1
	s_lshl_b32 s21, s21, 7
	s_and_b32 s21, s21, 0x780
	s_or_b32 s21, s21, s14
	s_or_b32 s22, s21, 0x20000
	s_waitcnt lgkmcnt(11)
	v_mfma_f32_16x16x32_bf16 v[174:177], v[178:181], v[206:209], v[174:177]
	v_mfma_f32_16x16x32_bf16 v[170:173], v[194:197], v[206:209], v[170:173]
	v_mfma_f32_16x16x32_bf16 v[158:161], v[198:201], v[206:209], v[158:161]
	v_mfma_f32_16x16x32_bf16 v[142:145], v[202:205], v[206:209], v[142:145]
	s_waitcnt lgkmcnt(10)
	v_mfma_f32_16x16x32_bf16 v[166:169], v[178:181], v[210:213], v[166:169]
	v_mfma_f32_16x16x32_bf16 v[162:165], v[194:197], v[210:213], v[162:165]
	buffer_load_dwordx4 v[2:5], v188, s[0:3], s21 offen
	v_mfma_f32_16x16x32_bf16 v[146:149], v[198:201], v[210:213], v[146:149]
	v_mfma_f32_16x16x32_bf16 v[122:125], v[202:205], v[210:213], v[122:125]
	s_waitcnt lgkmcnt(9)
	v_mfma_f32_16x16x32_bf16 v[154:157], v[178:181], v[214:217], v[154:157]
	v_mfma_f32_16x16x32_bf16 v[150:153], v[194:197], v[214:217], v[150:153]
	v_mfma_f32_16x16x32_bf16 v[130:133], v[198:201], v[214:217], v[130:133]
	v_mfma_f32_16x16x32_bf16 v[106:109], v[202:205], v[214:217], v[106:109]
	s_waitcnt lgkmcnt(8)
	v_mfma_f32_16x16x32_bf16 v[138:141], v[178:181], v[218:221], v[138:141]
	v_mfma_f32_16x16x32_bf16 v[134:137], v[194:197], v[218:221], v[134:137]
	buffer_load_dwordx4 v[6:9], v188, s[0:3], s22 offen
	s_or_b32 s22, s21, 0x40000
	s_or_b32 s21, s21, 0x60000
	v_mfma_f32_16x16x32_bf16 v[114:117], v[198:201], v[218:221], v[114:117]
	v_mfma_f32_16x16x32_bf16 v[90:93], v[202:205], v[218:221], v[90:93]
	s_waitcnt lgkmcnt(7)
	v_mfma_f32_16x16x32_bf16 v[126:129], v[178:181], v[222:225], v[126:129]
	v_mfma_f32_16x16x32_bf16 v[118:121], v[194:197], v[222:225], v[118:121]
	v_mfma_f32_16x16x32_bf16 v[98:101], v[198:201], v[222:225], v[98:101]
	v_mfma_f32_16x16x32_bf16 v[74:77], v[202:205], v[222:225], v[74:77]
	s_waitcnt lgkmcnt(6)
	v_mfma_f32_16x16x32_bf16 v[110:113], v[178:181], v[226:229], v[110:113]
	v_mfma_f32_16x16x32_bf16 v[102:105], v[194:197], v[226:229], v[102:105]
	buffer_load_dwordx4 v[14:17], v188, s[0:3], s22 offen
	v_mfma_f32_16x16x32_bf16 v[82:85], v[198:201], v[226:229], v[82:85]
	v_mfma_f32_16x16x32_bf16 v[62:65], v[202:205], v[226:229], v[62:65]
	s_waitcnt lgkmcnt(5)
	v_mfma_f32_16x16x32_bf16 v[94:97], v[178:181], v[230:233], v[94:97]
	v_mfma_f32_16x16x32_bf16 v[86:89], v[194:197], v[230:233], v[86:89]
	v_mfma_f32_16x16x32_bf16 v[70:73], v[198:201], v[230:233], v[70:73]
	v_mfma_f32_16x16x32_bf16 v[54:57], v[202:205], v[230:233], v[54:57]
	s_waitcnt lgkmcnt(4)
	v_mfma_f32_16x16x32_bf16 v[78:81], v[178:181], v[234:237], v[78:81]
	v_mfma_f32_16x16x32_bf16 v[66:69], v[194:197], v[234:237], v[66:69]
	buffer_load_dwordx4 v[26:29], v188, s[0:3], s21 offen
	v_mfma_f32_16x16x32_bf16 v[58:61], v[198:201], v[234:237], v[58:61]
	v_mfma_f32_16x16x32_bf16 v[50:53], v[202:205], v[234:237], v[50:53]
	s_setprio 0
	s_branch .LBB1_3
